# P1: conversion workgroups take all expert-weight tiles, GEMM workgroups skip their conversion tail
# speedup vs baseline: 1.0091x; 1.0042x over previous
.LBB0_533:
	s_branch .LBB0_632
	s_and_b32 s0, s56, 0xffffffe0
	s_cmp_lg_u32 s0, 32
	s_cbranch_scc1 .LBB0_577
	v_mov_b32_e32 v66, v0
	s_lshl_b32 s0, s56, 6
	v_ashrrev_i32_e32 v2, 1, v66
	v_lshlrev_b32_e32 v1, 2, v66
	v_and_b32_e32 v98, -8, v2
	s_and_b32 s0, s0, 0x7c0
	v_and_b32_e32 v1, 60, v1
	v_ashrrev_i32_e32 v99, 31, v98
	v_or_b32_e32 v4, s0, v1
	v_lshlrev_b64 v[2:3], 13, v[98:99]
	v_lshl_add_u64 v[2:3], s[76:77], 0, v[2:3]
	v_lshlrev_b32_e32 v100, 2, v4
	v_mov_b32_e32 v101, 0
	v_lshl_add_u64 v[58:59], v[2:3], 0, v[100:101]
	s_mov_b32 s0, 0x1d000000
	v_add_co_u32_e32 v2, vcc, s0, v58
	s_mov_b32 s0, 0x1d002000
	s_nop 0
	v_addc_co_u32_e32 v3, vcc, 0, v59, vcc
	v_add_co_u32_e32 v6, vcc, s0, v58
	s_mov_b32 s0, 0x1d004000
	s_nop 0
	v_addc_co_u32_e32 v7, vcc, 0, v59, vcc
	v_add_co_u32_e32 v10, vcc, s0, v58
	s_mov_b32 s0, 0x1d006000
	s_nop 0
	v_addc_co_u32_e32 v11, vcc, 0, v59, vcc
	v_add_co_u32_e32 v14, vcc, s0, v58
	s_mov_b32 s0, 0x1d008000
	s_nop 0
	v_addc_co_u32_e32 v15, vcc, 0, v59, vcc
	v_add_co_u32_e32 v18, vcc, s0, v58
	s_mov_b32 s0, 0x1d00a000
	s_nop 0
	v_addc_co_u32_e32 v19, vcc, 0, v59, vcc
	v_add_co_u32_e32 v22, vcc, s0, v58
	s_mov_b32 s0, 0x1d00c000
	s_nop 0
	v_addc_co_u32_e32 v23, vcc, 0, v59, vcc
	v_add_co_u32_e32 v26, vcc, s0, v58
	s_mov_b32 s0, 0x1d00e000
	s_nop 0
	v_addc_co_u32_e32 v27, vcc, 0, v59, vcc
	v_add_co_u32_e32 v28, vcc, s0, v58
	s_mov_b32 s0, 0x1d200000
	s_nop 0
	v_addc_co_u32_e32 v29, vcc, 0, v59, vcc
	global_load_dwordx4 v[2:5], v[2:3], off nt
	s_nop 0
	global_load_dwordx4 v[6:9], v[6:7], off nt
	s_nop 0
	global_load_dwordx4 v[10:13], v[10:11], off nt
	s_nop 0
	global_load_dwordx4 v[14:17], v[14:15], off nt
	s_nop 0
	global_load_dwordx4 v[18:21], v[18:19], off nt
	s_nop 0
	global_load_dwordx4 v[22:25], v[22:23], off nt
	s_nop 0
	global_load_dwordx4 v[30:33], v[26:27], off nt
	global_load_dwordx4 v[38:41], v[28:29], off nt
	v_add_co_u32_e32 v26, vcc, s0, v58
	s_mov_b32 s0, 0x1d202000
	s_nop 0
	v_addc_co_u32_e32 v27, vcc, 0, v59, vcc
	v_add_co_u32_e32 v34, vcc, s0, v58
	s_mov_b32 s0, 0x1d204000
	s_nop 0
	v_addc_co_u32_e32 v35, vcc, 0, v59, vcc
	v_add_co_u32_e32 v42, vcc, s0, v58
	s_mov_b32 s0, 0x1d206000
	s_nop 0
	v_addc_co_u32_e32 v43, vcc, 0, v59, vcc
	v_add_co_u32_e32 v46, vcc, s0, v58
	s_mov_b32 s0, 0x1d208000
	s_nop 0
	v_addc_co_u32_e32 v47, vcc, 0, v59, vcc
	v_add_co_u32_e32 v50, vcc, s0, v58
	s_mov_b32 s0, 0x1d20a000
	s_nop 0
	v_addc_co_u32_e32 v51, vcc, 0, v59, vcc
	v_add_co_u32_e32 v54, vcc, s0, v58
	s_mov_b32 s0, 0x1d20c000
	s_nop 0
	v_addc_co_u32_e32 v55, vcc, 0, v59, vcc
	v_add_co_u32_e32 v60, vcc, s0, v58
	s_mov_b32 s0, 0x1d20e000
	s_nop 0
	v_addc_co_u32_e32 v61, vcc, 0, v59, vcc
	v_add_co_u32_e32 v62, vcc, s0, v58
	global_load_dwordx4 v[26:29], v[26:27], off nt
	s_nop 0
	global_load_dwordx4 v[34:37], v[34:35], off nt
	v_addc_co_u32_e32 v63, vcc, 0, v59, vcc
	global_load_dwordx4 v[42:45], v[42:43], off nt
	s_nop 0
	global_load_dwordx4 v[46:49], v[46:47], off nt
	s_nop 0
	global_load_dwordx4 v[50:53], v[50:51], off nt
	s_nop 0
	global_load_dwordx4 v[54:57], v[54:55], off nt
	s_nop 0
	global_load_dwordx4 v[58:61], v[60:61], off nt
	s_nop 0
	global_load_dwordx4 v[62:65], v[62:63], off nt
	v_ashrrev_i32_e32 v67, 3, v66
	v_lshlrev_b32_e32 v68, 4, v66
	v_ashrrev_i32_e32 v104, 4, v66
	v_add_u32_e32 v66, 0x200, v66
	v_and_b32_e32 v67, -2, v67
	s_movk_i32 s0, 0x104
	v_ashrrev_i32_e32 v106, 4, v66
	s_mov_b32 s5, 0
	v_mul_u32_u24_e32 v99, 0x104, v1
	v_and_b32_e32 v102, 0xf0, v68
	v_mov_b32_e32 v103, v101
	v_mul_lo_u32 v105, v104, s0
	v_mul_lo_u32 v107, v106, s0
	s_add_i32 s16, s56, 0x5d60
	v_mov_b32_e32 v108, 0x7c
	v_lshlrev_b32_e32 v109, 2, v67
	s_mov_b32 s17, 0
	s_branch .LBB0_538

.LBB0_632:
	s_and_b64 vcc, exec, s[34:35]
	s_cbranch_vccz .LBB0_688
	s_ashr_i32 s0, s96, 6
	s_mul_i32 s3, s0, 24
	s_add_i32 s0, s89, s3
	s_sub_i32 s10, s0, 40
	s_waitcnt vmcnt(0)
	v_mov_b32_e32 v17, 0
	s_cmpk_lt_i32 s10, 0x6000
	v_mov_b32_e32 v66, v0
	s_cselect_b64 s[4:5], -1, 0
	s_cmpk_gt_i32 s10, 0x5fff
	v_mov_b32_e32 v16, v17
	v_mov_b32_e32 v15, v17
	v_mov_b32_e32 v14, v17
	v_mov_b32_e32 v33, v17
	v_mov_b32_e32 v32, v17
	v_mov_b32_e32 v31, v17
	v_mov_b32_e32 v30, v17
	v_mov_b32_e32 v25, v17
	v_mov_b32_e32 v24, v17
	v_mov_b32_e32 v23, v17
	v_mov_b32_e32 v22, v17
	v_mov_b32_e32 v29, v17
	v_mov_b32_e32 v28, v17
	v_mov_b32_e32 v27, v17
	v_mov_b32_e32 v26, v17
	v_mov_b32_e32 v13, v17
	v_mov_b32_e32 v12, v17
	v_mov_b32_e32 v11, v17
	v_mov_b32_e32 v10, v17
	v_mov_b32_e32 v21, v17
	v_mov_b32_e32 v20, v17
	v_mov_b32_e32 v19, v17
	v_mov_b32_e32 v18, v17
	v_mov_b32_e32 v5, v17
	v_mov_b32_e32 v4, v17
	v_mov_b32_e32 v3, v17
	v_mov_b32_e32 v2, v17
	v_mov_b32_e32 v9, v17
	v_mov_b32_e32 v8, v17
	v_mov_b32_e32 v7, v17
	v_mov_b32_e32 v6, v17
	s_cbranch_scc1 .LBB0_640
	s_cmpk_lt_i32 s10, 0x4000
	s_cselect_b64 s[0:1], -1, 0
	s_cmpk_gt_i32 s10, 0x3fff
	s_cbranch_scc0 .LBB0_637
	s_add_i32 s6, s10, 0xffffc000
	s_lshr_b32 s6, s6, 8
	s_mov_b32 s7, 0
	s_and_b32 s11, s10, 0xff
	s_lshl_b64 s[6:7], s[6:7], 24
	s_add_u32 s6, s76, s6
	s_addc_u32 s7, s77, s7
	s_cbranch_execz .LBB0_638
	s_mov_b32 s12, 32
	s_mov_b64 s[8:9], 0x800
	s_branch .LBB0_639

.LBB0_640:
	s_ashr_i32 s11, s43, 6
	s_mul_i32 s17, s11, 24
	s_add_i32 s12, s17, s10
	s_cmpk_gt_i32 s12, 0x5fff
	s_cbranch_scc1 .LBB0_647
	s_cmpk_lt_i32 s12, 0x4000
	s_cselect_b64 s[0:1], -1, 0
	s_cmpk_gt_i32 s12, 0x3fff
	s_cbranch_scc0 .LBB0_644
	s_add_i32 s6, s12, 0xffffc000
	s_lshr_b32 s6, s6, 8
	s_mov_b32 s7, 0
	s_and_b32 s10, s12, 0xff
	s_lshl_b64 s[6:7], s[6:7], 24
	s_add_u32 s6, s76, s6
	s_addc_u32 s7, s77, s7
	s_cbranch_execz .LBB0_645
	s_mov_b32 s12, 32
	s_mov_b64 s[8:9], 0x800
	s_branch .LBB0_646

.LBB0_650:
	s_mov_b32 s100, 1
	s_add_i32 s3, s3, s12
	s_add_i32 s0, s89, s3
	s_sub_i32 s0, s0, 40
	s_cmpk_lt_i32 s0, 0x6000
	s_cbranch_scc0 .LBB0_687
.LBB0_651:
	s_add_i32 s23, s20, s3
	s_sub_i32 s22, s23, 40
	s_cmpk_lt_i32 s22, 0x6000
	s_cselect_b64 s[6:7], -1, 0
	s_cmpk_gt_i32 s22, 0x5fff
	s_cbranch_scc1 .Lmy_c1_skip
	s_cmpk_lt_i32 s22, 0x4000
	s_cselect_b64 s[0:1], -1, 0
	s_cmpk_gt_i32 s22, 0x3fff
	s_mov_b64 s[10:11], -1
	s_cbranch_scc0 .LBB0_654
	s_add_i32 s4, s23, 0xffffbfd8
	s_lshr_b32 s4, s4, 8
	s_and_b32 s24, s22, 0xff
	s_lshl_b64 s[8:9], s[4:5], 24
	s_add_u32 s8, s76, s8
	s_addc_u32 s9, s77, s9
	s_mov_b64 s[10:11], 0

.LBB0_662:
	v_mul_f32_e32 v100, 0x42800000, v6
	v_mul_f32_e32 v111, 0x42800000, v2
	v_mov_b32_e32 v110, 0
	v_cvt_pk_fp8_f32 v110, v100, v111
	v_mul_f32_e32 v100, 0x42800000, v26
	v_mul_f32_e32 v114, 0x42800000, v22
	v_mov_b32_e32 v111, 0
	v_cvt_pk_fp8_f32 v111, v100, v114
	v_mul_f32_e32 v112, 0x42800000, v18
	v_mul_f32_e32 v113, 0x42800000, v10
	v_cvt_pk_fp8_f32 v110, v112, v113 op_sel:[0,0,1]
	v_mul_f32_e32 v100, 0x42800000, v30
	v_mul_f32_e32 v112, 0x42800000, v14
	v_cvt_pk_fp8_f32 v111, v100, v112 op_sel:[0,0,1]
	v_mul_f32_e32 v100, 0x42800000, v7
	v_mul_f32_e32 v112, 0x42800000, v3
	v_mov_b32_e32 v115, 0
	v_cvt_pk_fp8_f32 v115, v100, v112
	v_mul_f32_e32 v100, 0x42800000, v27
	v_mul_f32_e32 v112, 0x42800000, v23
	v_mov_b32_e32 v116, 0
	v_cvt_pk_fp8_f32 v116, v100, v112
	v_mul_f32_e32 v113, 0x42800000, v19
	v_mul_f32_e32 v114, 0x42800000, v11
	v_mul_f32_e32 v100, 0x42800000, v31
	v_mul_f32_e32 v112, 0x42800000, v15
	v_cvt_pk_fp8_f32 v115, v113, v114 op_sel:[0,0,1]
	v_cvt_pk_fp8_f32 v116, v100, v112 op_sel:[0,0,1]
	v_mul_f32_e32 v100, 0x42800000, v8
	v_mul_f32_e32 v113, 0x42800000, v4
	v_mov_b32_e32 v112, 0
	v_cvt_pk_fp8_f32 v112, v100, v113
	v_mul_f32_e32 v100, 0x42800000, v28
	v_mul_f32_e32 v118, 0x42800000, v24
	v_mov_b32_e32 v113, 0
	v_cvt_pk_fp8_f32 v113, v100, v118
	v_mul_f32_e32 v114, 0x42800000, v20
	v_mul_f32_e32 v117, 0x42800000, v12
	v_cvt_pk_fp8_f32 v112, v114, v117 op_sel:[0,0,1]
	v_mul_f32_e32 v100, 0x42800000, v32
	v_mul_f32_e32 v114, 0x42800000, v16
	v_cvt_pk_fp8_f32 v113, v100, v114 op_sel:[0,0,1]
	v_mul_f32_e32 v100, 0x42800000, v9
	v_mul_f32_e32 v114, 0x42800000, v5
	v_mov_b32_e32 v119, 0
	v_cvt_pk_fp8_f32 v119, v100, v114
	v_mul_f32_e32 v100, 0x42800000, v29
	v_mul_f32_e32 v114, 0x42800000, v25
	v_mov_b32_e32 v120, 0
	v_cvt_pk_fp8_f32 v120, v100, v114
	s_mul_i32 s9, s21, 0x4100
	v_mul_f32_e32 v117, 0x42800000, v21
	v_mul_f32_e32 v118, 0x42800000, v13
	v_mul_f32_e32 v100, 0x42800000, v33
	v_mul_f32_e32 v114, 0x42800000, v17
	s_add_i32 s8, s4, -1
	s_add_i32 s9, s9, 0
	v_cvt_pk_fp8_f32 v119, v117, v118 op_sel:[0,0,1]
	v_cvt_pk_fp8_f32 v120, v100, v114 op_sel:[0,0,1]
	s_and_b32 s8, s10, s8
	v_add3_u32 v100, s9, v109, v103
	s_lshl_b32 s8, s8, 6
	ds_write2_b32 v100, v115, v116 offset0:65 offset1:66
	ds_write2_b64 v100, v[110:111], v[112:113] offset1:65
	ds_write2_b32 v100, v119, v120 offset0:195 offset1:196
	v_add_u32_e32 v100, s9, v98
	s_waitcnt lgkmcnt(0)
	s_barrier
	v_add_u32_e32 v112, v100, v105
	v_add_u32_e32 v114, s8, v104
	s_ff1_i32_b32 s4, s4
	ds_read2_b32 v[110:111], v112 offset1:1
	ds_read2_b32 v[112:113], v112 offset0:2 offset1:3
	v_ashrrev_i32_e32 v115, 31, v114
	s_lshr_b32 s4, s10, s4
	v_lshlrev_b64 v[114:115], 11, v[114:115]
	s_lshl_b32 s4, s4, 8
	v_lshl_add_u64 v[114:115], s[0:1], 0, v[114:115]
	v_lshl_add_u64 v[114:115], v[114:115], 0, s[4:5]
	v_lshl_add_u64 v[118:119], v[114:115], 0, v[98:99]
	v_add_u32_e32 v100, v100, v107
	ds_read2_b32 v[114:115], v100 offset1:1
	ds_read2_b32 v[116:117], v100 offset0:2 offset1:3
	s_waitcnt lgkmcnt(2)
	global_store_dwordx4 v[118:119], v[110:113], off nt
	s_nop 1
	v_add_u32_e32 v110, s8, v106
	v_ashrrev_i32_e32 v111, 31, v110
	v_lshlrev_b64 v[110:111], 11, v[110:111]
	v_lshl_add_u64 v[110:111], s[0:1], 0, v[110:111]
	v_lshl_add_u64 v[110:111], v[110:111], 0, s[4:5]
	s_add_i32 s4, s19, s3
	s_sub_i32 s24, s4, 40
	v_lshl_add_u64 v[110:111], v[110:111], 0, v[98:99]
	s_cmpk_gt_i32 s24, 0x5fff
	s_waitcnt lgkmcnt(0)
	global_store_dwordx4 v[110:111], v[114:117], off nt
	s_cbranch_scc1 .Lmy_c2_skip
	s_cmpk_lt_i32 s24, 0x4000
	s_cselect_b64 s[0:1], -1, 0
	s_cmpk_gt_i32 s24, 0x3fff
	s_mov_b64 s[10:11], -1
	s_cbranch_scc0 .LBB0_665
	s_addk_i32 s4, 0xbfd8
	s_lshr_b32 s4, s4, 8
	s_and_b32 s25, s24, 0xff
	s_lshl_b64 s[8:9], s[4:5], 24
	s_add_u32 s8, s76, s8
	s_addc_u32 s9, s77, s9
	s_mov_b64 s[10:11], 0

.LBB0_669:
	s_add_i32 s4, s17, s3
	s_xor_b32 s10, s21, 1
	s_sub_i32 s24, s4, 40
	s_cmpk_gt_i32 s24, 0x5fff
	s_cbranch_scc1 .LBB0_675
	s_cmpk_gt_i32 s24, 0x3fff
	s_mov_b64 s[8:9], -1
	s_cbranch_scc0 .LBB0_672
	s_addk_i32 s4, 0xbfd8
	s_lshr_b32 s4, s4, 8
	s_and_b32 s11, s24, 0xff
	s_lshl_b64 s[0:1], s[4:5], 22
	s_add_u32 s0, s13, s0
	s_addc_u32 s1, s14, s1
	s_mov_b64 s[8:9], 0

.LBB0_674:
	v_mul_f32_e32 v100, 0x42800000, v34
	v_mul_f32_e32 v111, 0x42800000, v38
	v_mov_b32_e32 v110, v101
	v_cvt_pk_fp8_f32 v110, v100, v111
	v_mul_f32_e32 v100, 0x42800000, v50
	v_mul_f32_e32 v114, 0x42800000, v54
	v_mov_b32_e32 v111, v101
	v_cvt_pk_fp8_f32 v111, v100, v114
	v_mul_f32_e32 v112, 0x42800000, v42
	v_mul_f32_e32 v113, 0x42800000, v46
	v_cvt_pk_fp8_f32 v110, v112, v113 op_sel:[0,0,1]
	v_mul_f32_e32 v100, 0x42800000, v58
	v_mul_f32_e32 v112, 0x42800000, v62
	v_cvt_pk_fp8_f32 v111, v100, v112 op_sel:[0,0,1]
	v_mul_f32_e32 v100, 0x42800000, v35
	v_mul_f32_e32 v112, 0x42800000, v39
	v_mov_b32_e32 v115, v101
	v_cvt_pk_fp8_f32 v115, v100, v112
	v_mul_f32_e32 v100, 0x42800000, v51
	v_mul_f32_e32 v112, 0x42800000, v55
	v_mov_b32_e32 v116, v101
	v_cvt_pk_fp8_f32 v116, v100, v112
	v_mul_f32_e32 v113, 0x42800000, v43
	v_mul_f32_e32 v114, 0x42800000, v47
	v_mul_f32_e32 v100, 0x42800000, v59
	v_mul_f32_e32 v112, 0x42800000, v63
	v_cvt_pk_fp8_f32 v115, v113, v114 op_sel:[0,0,1]
	v_cvt_pk_fp8_f32 v116, v100, v112 op_sel:[0,0,1]
	v_mul_f32_e32 v100, 0x42800000, v36
	v_mul_f32_e32 v113, 0x42800000, v40
	v_mov_b32_e32 v112, v101
	v_cvt_pk_fp8_f32 v112, v100, v113
	v_mul_f32_e32 v100, 0x42800000, v52
	v_mul_f32_e32 v118, 0x42800000, v56
	v_mov_b32_e32 v113, v101
	v_cvt_pk_fp8_f32 v113, v100, v118
	v_mul_f32_e32 v114, 0x42800000, v44
	v_mul_f32_e32 v117, 0x42800000, v48
	v_cvt_pk_fp8_f32 v112, v114, v117 op_sel:[0,0,1]
	v_mul_f32_e32 v100, 0x42800000, v60
	v_mul_f32_e32 v114, 0x42800000, v64
	v_cvt_pk_fp8_f32 v113, v100, v114 op_sel:[0,0,1]
	v_mul_f32_e32 v100, 0x42800000, v37
	v_mul_f32_e32 v114, 0x42800000, v41
	v_mov_b32_e32 v119, v101
	v_cvt_pk_fp8_f32 v119, v100, v114
	v_mul_f32_e32 v100, 0x42800000, v53
	v_mul_f32_e32 v114, 0x42800000, v57
	v_mov_b32_e32 v120, v101
	v_cvt_pk_fp8_f32 v120, v100, v114
	s_mulk_i32 s10, 0x4100
	v_mul_f32_e32 v117, 0x42800000, v45
	v_mul_f32_e32 v118, 0x42800000, v49
	v_mul_f32_e32 v100, 0x42800000, v61
	v_mul_f32_e32 v114, 0x42800000, v65
	s_add_i32 s8, s4, -1
	s_add_i32 s9, s10, 0
	v_cvt_pk_fp8_f32 v119, v117, v118 op_sel:[0,0,1]
	v_cvt_pk_fp8_f32 v120, v100, v114 op_sel:[0,0,1]
	s_and_b32 s8, s11, s8
	v_add3_u32 v100, s9, v109, v103
	s_lshl_b32 s8, s8, 6
	ds_write2_b32 v100, v115, v116 offset0:65 offset1:66
	ds_write2_b64 v100, v[110:111], v[112:113] offset1:65
	ds_write2_b32 v100, v119, v120 offset0:195 offset1:196
	v_add_u32_e32 v100, s9, v98
	s_waitcnt lgkmcnt(0)
	s_barrier
	v_add_u32_e32 v112, v100, v105
	v_add_u32_e32 v114, s8, v104
	s_ff1_i32_b32 s4, s4
	ds_read2_b32 v[110:111], v112 offset1:1
	ds_read2_b32 v[112:113], v112 offset0:2 offset1:3
	v_ashrrev_i32_e32 v115, 31, v114
	s_lshr_b32 s4, s11, s4
	v_lshlrev_b64 v[114:115], 11, v[114:115]
	s_lshl_b32 s4, s4, 8
	v_lshl_add_u64 v[114:115], s[0:1], 0, v[114:115]
	v_lshl_add_u64 v[114:115], v[114:115], 0, s[4:5]
	v_lshl_add_u64 v[118:119], v[114:115], 0, v[98:99]
	v_add_u32_e32 v100, v100, v107
	ds_read2_b32 v[114:115], v100 offset1:1
	ds_read2_b32 v[116:117], v100 offset0:2 offset1:3
	s_waitcnt lgkmcnt(2)
	global_store_dwordx4 v[118:119], v[110:113], off nt
	s_nop 1
	v_add_u32_e32 v110, s8, v106
	v_ashrrev_i32_e32 v111, 31, v110
	v_lshlrev_b64 v[110:111], 11, v[110:111]
	v_lshl_add_u64 v[110:111], s[0:1], 0, v[110:111]
	v_lshl_add_u64 v[110:111], v[110:111], 0, s[4:5]
	v_lshl_add_u64 v[110:111], v[110:111], 0, v[98:99]
	s_waitcnt lgkmcnt(0)
	global_store_dwordx4 v[110:111], v[114:117], off nt
	s_add_i32 s4, s18, s3
	s_sub_i32 s25, s4, 40
	s_cmpk_gt_i32 s25, 0x5fff
	s_cbranch_scc0 .LBB0_676
	s_branch .Lmy_c3_skip
.LBB0_675:
	s_mov_b32 s21, s10
	s_add_i32 s4, s18, s3
	s_sub_i32 s25, s4, 40
	s_cmpk_gt_i32 s25, 0x5fff
	s_cbranch_scc1 .Lmy_c3_skip
